# prefetch weights at start of B, M, N (blocking)
# baseline (speedup 1.0000x reference)
.LBB0_5188:
	v_readlane_b32 s2, v254, 0
	v_readlane_b32 s3, v254, 1
	s_load_dword s0, s[2:3], 0x128
	v_readlane_b32 s4, v254, 50
	s_add_i32 s40, s4, 12
	s_waitcnt lgkmcnt(0)
	s_cmp_le_i32 s0, s40
	s_cbranch_scc0 .LBB0_6074
	s_load_dword s0, s[2:3], 0x12c
	s_waitcnt lgkmcnt(0)
	s_cmp_ge_i32 s40, s0
	s_cbranch_scc1 .LBB0_6074
	v_readlane_b32 s12, v254, 0
	v_readlane_b32 s13, v254, 1
	s_load_dwordx2 s[72:73], s[12:13], 0x120
	v_lshlrev_b32_e32 v0, 4, v235
	s_waitcnt lgkmcnt(0)
	s_mul_i32 s12, s48, 0x4000000
	s_mul_i32 s13, s43, 0x40000
	s_add_u32 s12, s12, s13
	s_add_u32 s12, s12, 0x8e00000
	s_add_u32 s54, s72, s12
	s_addc_u32 s55, s73, 0
	v_mov_b32_e32 v3, v0
	global_load_dwordx4 v[4:7], v3, s[54:55]
	v_add_u32_e32 v3, 0x2000, v3
	global_load_dwordx4 v[8:11], v3, s[54:55]
	v_add_u32_e32 v3, 0x2000, v3
	global_load_dwordx4 v[12:15], v3, s[54:55]
	v_add_u32_e32 v3, 0x2000, v3
	global_load_dwordx4 v[16:19], v3, s[54:55]
	v_add_u32_e32 v3, 0x2000, v3
	global_load_dwordx4 v[20:23], v3, s[54:55]
	v_add_u32_e32 v3, 0x2000, v3
	global_load_dwordx4 v[24:27], v3, s[54:55]
	v_add_u32_e32 v3, 0x2000, v3
	global_load_dwordx4 v[28:31], v3, s[54:55]
	v_add_u32_e32 v3, 0x2000, v3
	global_load_dwordx4 v[32:35], v3, s[54:55]
	v_add_u32_e32 v3, 0x2000, v3
	s_waitcnt vmcnt(0)
	global_load_dwordx4 v[4:7], v3, s[54:55]
	v_add_u32_e32 v3, 0x2000, v3
	global_load_dwordx4 v[8:11], v3, s[54:55]
	v_add_u32_e32 v3, 0x2000, v3
	global_load_dwordx4 v[12:15], v3, s[54:55]
	v_add_u32_e32 v3, 0x2000, v3
	global_load_dwordx4 v[16:19], v3, s[54:55]
	v_add_u32_e32 v3, 0x2000, v3
	global_load_dwordx4 v[20:23], v3, s[54:55]
	v_add_u32_e32 v3, 0x2000, v3
	global_load_dwordx4 v[24:27], v3, s[54:55]
	v_add_u32_e32 v3, 0x2000, v3
	global_load_dwordx4 v[28:31], v3, s[54:55]
	v_add_u32_e32 v3, 0x2000, v3
	global_load_dwordx4 v[32:35], v3, s[54:55]
	v_add_u32_e32 v3, 0x2000, v3
	s_waitcnt vmcnt(0)
	global_load_dwordx4 v[4:7], v3, s[54:55]
	v_add_u32_e32 v3, 0x2000, v3
	global_load_dwordx4 v[8:11], v3, s[54:55]
	v_add_u32_e32 v3, 0x2000, v3
	global_load_dwordx4 v[12:15], v3, s[54:55]
	v_add_u32_e32 v3, 0x2000, v3
	global_load_dwordx4 v[16:19], v3, s[54:55]
	v_add_u32_e32 v3, 0x2000, v3
	global_load_dwordx4 v[20:23], v3, s[54:55]
	v_add_u32_e32 v3, 0x2000, v3
	global_load_dwordx4 v[24:27], v3, s[54:55]
	v_add_u32_e32 v3, 0x2000, v3
	global_load_dwordx4 v[28:31], v3, s[54:55]
	v_add_u32_e32 v3, 0x2000, v3
	global_load_dwordx4 v[32:35], v3, s[54:55]
	v_add_u32_e32 v3, 0x2000, v3
	s_waitcnt vmcnt(0)
	global_load_dwordx4 v[4:7], v3, s[54:55]
	v_add_u32_e32 v3, 0x2000, v3
	global_load_dwordx4 v[8:11], v3, s[54:55]
	v_add_u32_e32 v3, 0x2000, v3
	global_load_dwordx4 v[12:15], v3, s[54:55]
	v_add_u32_e32 v3, 0x2000, v3
	global_load_dwordx4 v[16:19], v3, s[54:55]
	v_add_u32_e32 v3, 0x2000, v3
	global_load_dwordx4 v[20:23], v3, s[54:55]
	v_add_u32_e32 v3, 0x2000, v3
	global_load_dwordx4 v[24:27], v3, s[54:55]
	v_add_u32_e32 v3, 0x2000, v3
	global_load_dwordx4 v[28:31], v3, s[54:55]
	v_add_u32_e32 v3, 0x2000, v3
	global_load_dwordx4 v[32:35], v3, s[54:55]
	v_add_u32_e32 v3, 0x2000, v3
	s_waitcnt vmcnt(0)
	v_readlane_b32 s8, v254, 0
	v_readlane_b32 s9, v254, 1
	s_load_dwordx2 s[10:11], s[8:9], 0x120
	s_mov_b32 s0, s43
	v_mov_b32_e32 v216, v235
	v_readlane_b32 s33, v254, 6
	s_cmp_lg_u32 s33, 0
	v_and_b32_e32 v217, 63, v216
	s_cbranch_scc1 .LBB0_5198
	v_cmp_gt_u32_e64 s[2:3], 16, v217
	v_mov_b32_e32 v0, 0
	s_and_saveexec_b64 s[4:5], s[2:3]
	s_cbranch_execz .LBB0_5193
	s_lshl_b64 s[6:7], s[16:17], 2
	s_waitcnt lgkmcnt(0)
	s_add_u32 s6, s10, s6
	s_addc_u32 s7, s11, s7
	v_lshlrev_b32_e32 v0, 8, v217
	v_lshl_add_u64 v[2:3], s[6:7], 0, v[0:1]
	v_add_co_u32_e32 v2, vcc, 0x10000, v2
	s_nop 1
	v_addc_co_u32_e32 v3, vcc, 0, v3, vcc
	global_load_dword v0, v[2:3], off
	v_mov_b32_e32 v2, 0x4000
	s_waitcnt vmcnt(0)
	v_med3_i32 v0, v0, 0, v2

.LBB0_6134:
	v_readlane_b32 s2, v254, 0
	v_readlane_b32 s3, v254, 1
	s_load_dword s0, s[2:3], 0x128
	v_readlane_b32 s4, v254, 50
	s_add_i32 s36, s4, 13
	s_waitcnt lgkmcnt(0)
	s_cmp_le_i32 s0, s36
	s_cbranch_scc0 .LBB0_6987
	s_load_dword s0, s[2:3], 0x12c
	s_waitcnt lgkmcnt(0)
	s_cmp_ge_i32 s36, s0
	s_cbranch_scc1 .LBB0_6987
	v_readlane_b32 s12, v254, 0
	v_readlane_b32 s13, v254, 1
	s_load_dwordx2 s[72:73], s[12:13], 0x120
	v_lshlrev_b32_e32 v0, 4, v235
	s_waitcnt lgkmcnt(0)
	s_mul_i32 s12, s48, 0x2000000
	s_mul_i32 s13, s43, 0x20000
	s_add_u32 s12, s12, s13
	s_add_u32 s12, s12, 0x10e00000
	s_add_u32 s54, s72, s12
	s_addc_u32 s55, s73, 0
	v_mov_b32_e32 v3, v0
	global_load_dwordx4 v[4:7], v3, s[54:55]
	v_add_u32_e32 v3, 0x2000, v3
	global_load_dwordx4 v[8:11], v3, s[54:55]
	v_add_u32_e32 v3, 0x2000, v3
	global_load_dwordx4 v[12:15], v3, s[54:55]
	v_add_u32_e32 v3, 0x2000, v3
	global_load_dwordx4 v[16:19], v3, s[54:55]
	v_add_u32_e32 v3, 0x2000, v3
	global_load_dwordx4 v[20:23], v3, s[54:55]
	v_add_u32_e32 v3, 0x2000, v3
	global_load_dwordx4 v[24:27], v3, s[54:55]
	v_add_u32_e32 v3, 0x2000, v3
	global_load_dwordx4 v[28:31], v3, s[54:55]
	v_add_u32_e32 v3, 0x2000, v3
	global_load_dwordx4 v[32:35], v3, s[54:55]
	v_add_u32_e32 v3, 0x2000, v3
	s_waitcnt vmcnt(0)
	global_load_dwordx4 v[4:7], v3, s[54:55]
	v_add_u32_e32 v3, 0x2000, v3
	global_load_dwordx4 v[8:11], v3, s[54:55]
	v_add_u32_e32 v3, 0x2000, v3
	global_load_dwordx4 v[12:15], v3, s[54:55]
	v_add_u32_e32 v3, 0x2000, v3
	global_load_dwordx4 v[16:19], v3, s[54:55]
	v_add_u32_e32 v3, 0x2000, v3
	global_load_dwordx4 v[20:23], v3, s[54:55]
	v_add_u32_e32 v3, 0x2000, v3
	global_load_dwordx4 v[24:27], v3, s[54:55]
	v_add_u32_e32 v3, 0x2000, v3
	global_load_dwordx4 v[28:31], v3, s[54:55]
	v_add_u32_e32 v3, 0x2000, v3
	global_load_dwordx4 v[32:35], v3, s[54:55]
	v_add_u32_e32 v3, 0x2000, v3
	s_waitcnt vmcnt(0)
	v_readlane_b32 s8, v254, 0
	v_readlane_b32 s9, v254, 1
	s_load_dwordx2 s[10:11], s[8:9], 0x120
	s_mov_b32 s6, s43
	v_mov_b32_e32 v216, v235
	v_readlane_b32 s33, v254, 6
	s_cmp_lg_u32 s33, 0
	v_and_b32_e32 v217, 63, v216
	s_cbranch_scc1 .LBB0_6144
	v_cmp_gt_u32_e64 s[2:3], 16, v217
	v_mov_b32_e32 v0, 0
	s_and_saveexec_b64 s[4:5], s[2:3]
	s_cbranch_execz .LBB0_6139
	s_lshl_b64 s[12:13], s[16:17], 2
	s_waitcnt lgkmcnt(0)
	s_add_u32 s12, s10, s12
	s_addc_u32 s13, s11, s13
	v_lshlrev_b32_e32 v0, 8, v217
	v_lshl_add_u64 v[2:3], s[12:13], 0, v[0:1]
	v_add_co_u32_e32 v2, vcc, 0x10000, v2
	s_nop 1
	v_addc_co_u32_e32 v3, vcc, 0, v3, vcc
	global_load_dword v0, v[2:3], off
	v_mov_b32_e32 v2, 0x4000
	s_waitcnt vmcnt(0)
	v_med3_i32 v0, v0, 0, v2
